# static s_setprio 1 for waves 0-3 (the other half) set once at kernel entry, per-phase flips removed
# speedup vs baseline: 1.0028x; 1.0028x over previous
; #define LAS __attribute__((address_space(3)))
; __global__ void __launch_bounds__(NWAVES * 64, 2) mk_fwd(Args args) {
;     extern __shared__ __attribute__((aligned(16))) unsigned char lds[];
;     Frame F;
;     F.lds = (LAS unsigned char*)lds; F.MISC = (volatile LAS unsigned*)(F.lds + MISC_OFF);
;     F.tid = threadIdx.x; F.lane = F.tid & 63; F.wave = __builtin_amdgcn_readfirstlane(F.tid >> 6);
_Z6mk_fwd4Args:
	v_readfirstlane_b32 s5, v0
	s_nop 3
	s_and_b32 s5, s5, 0x3ff
	s_lshr_b32 s5, s5, 6
	s_cmp_lt_u32 s5, 4
	s_cbranch_scc0 .Lprio_done
	s_setprio 1
